# attention loop: 14 adjacent v_fmamk_f32 pairs of the score scaling packed into v_pk_fma_f32 (constant from s[90:91], broadcast addend via op_sel) - 14 VALU issues fewer per iteration, bit-identical
# speedup vs baseline: 1.0134x; 1.0102x over previous
.LBB0_3261:
	v_cndmask_b32_e64 v215, v2, v215, s[10:11]
	v_mul_f32_e32 v145, 0xbe0293ee, v215
	v_fmamk_f32 v2, v114, 0x3e0293ee, v145
	v_fmamk_f32 v19, v115, 0x3e0293ee, v145
	v_pk_fma_f32 v[20:21], v[116:117], s[90:91], v[144:145] op_sel:[0,0,1] op_sel_hi:[1,0,1]
	v_pk_fma_f32 v[22:23], v[118:119], s[90:91], v[144:145] op_sel:[0,0,1] op_sel_hi:[1,0,1]
	v_pk_fma_f32 v[24:25], v[120:121], s[90:91], v[144:145] op_sel:[0,0,1] op_sel_hi:[1,0,1]
	v_pk_fma_f32 v[26:27], v[122:123], s[90:91], v[144:145] op_sel:[0,0,1] op_sel_hi:[1,0,1]
	v_pk_fma_f32 v[28:29], v[124:125], s[90:91], v[144:145] op_sel:[0,0,1] op_sel_hi:[1,0,1]
	v_pk_fma_f32 v[30:31], v[126:127], s[90:91], v[144:145] op_sel:[0,0,1] op_sel_hi:[1,0,1]
	v_pk_fma_f32 v[32:33], v[128:129], s[90:91], v[144:145] op_sel:[0,0,1] op_sel_hi:[1,0,1]
	v_exp_f32_e32 v142, v2
	v_exp_f32_e32 v144, v19
	v_exp_f32_e32 v140, v20
	v_exp_f32_e32 v143, v21
	v_exp_f32_e32 v138, v22
	v_exp_f32_e32 v141, v23
	v_exp_f32_e32 v137, v24
	v_exp_f32_e32 v139, v25
	v_exp_f32_e32 v134, v26
	v_exp_f32_e32 v136, v27
	v_exp_f32_e32 v132, v28
	v_exp_f32_e32 v135, v29
	v_exp_f32_e32 v130, v30
	v_exp_f32_e32 v133, v31
	v_exp_f32_e32 v2, v32
	v_exp_f32_e32 v131, v33
	v_pk_fma_f32 v[146:147], v[98:99], s[90:91], v[144:145] op_sel:[0,0,1] op_sel_hi:[1,0,1]
	v_pk_fma_f32 v[148:149], v[100:101], s[90:91], v[144:145] op_sel:[0,0,1] op_sel_hi:[1,0,1]
	v_pk_fma_f32 v[150:151], v[102:103], s[90:91], v[144:145] op_sel:[0,0,1] op_sel_hi:[1,0,1]
	v_pk_fma_f32 v[152:153], v[104:105], s[90:91], v[144:145] op_sel:[0,0,1] op_sel_hi:[1,0,1]
	v_pk_fma_f32 v[154:155], v[106:107], s[90:91], v[144:145] op_sel:[0,0,1] op_sel_hi:[1,0,1]
	v_pk_fma_f32 v[156:157], v[108:109], s[90:91], v[144:145] op_sel:[0,0,1] op_sel_hi:[1,0,1]
	v_pk_fma_f32 v[158:159], v[110:111], s[90:91], v[144:145] op_sel:[0,0,1] op_sel_hi:[1,0,1]
	v_fmamk_f32 v160, v112, 0x3e0293ee, v145
	v_fmac_f32_e32 v145, 0x3e0293ee, v113
	s_waitcnt lgkmcnt(0)
	s_barrier
	s_and_b32 s16, s92, 15
	s_cmp_lg_u32 s16, s80
	s_cselect_b64 s[10:11], -1, 0
	s_mov_b64 s[14:15], -1
	s_and_b64 vcc, exec, s[10:11]
	s_cbranch_vccz .LBB0_3265
	s_lshr_b32 s12, s83, s16
	s_bitcmp1_b32 s12, 0
	s_cselect_b64 s[12:13], -1, 0
	s_cbranch_execz .LBB0_3266
